# load de-serialisation: N2 row-loop constants (12 loads) requested together instead of four waited rounds; G2 epilogue requests the first eight residual rows before waiting on the gate loads
# speedup vs baseline: 1.0029x; 1.0029x over previous
.LBB0_699:
	s_mul_hi_i32 s11, s13, 0x78787879
	s_lshr_b32 s14, s11, 31
	s_ashr_i32 s11, s11, 3
	s_add_i32 s22, s11, s14
	s_mul_i32 s11, s22, 0xffffffef
	s_add_i32 s94, s11, s13
	s_cmp_lg_u32 s94, 0
	s_cselect_b64 s[96:97], -1, 0
	s_and_b64 s[14:15], s[96:97], exec
	s_cselect_b32 s11, s22, 8
	s_mul_hi_i32 s15, s11, 0x6000
	s_mulk_i32 s11, 0x6000
	s_add_u32 s14, s61, s11
	v_lshl_or_b32 v208, s10, 8, v224
	s_addc_u32 s15, s64, s15
	v_ashrrev_i32_e32 v209, 31, v208
	v_lshl_add_u64 v[6:7], v[208:209], 2, s[14:15]
	s_mov_b32 s10, 0x102000
	v_add_co_u32_e32 v2, vcc, s10, v6
	s_mov_b64 s[10:11], 0x102000
	s_nop 15
	s_nop 15
	s_nop 0
	v_addc_co_u32_e32 v3, vcc, 0, v7, vcc
	v_lshl_add_u64 v[14:15], v[6:7], 0, s[10:11]
	global_load_dwordx4 v[2:5], v[2:3], off
	s_nop 0
	global_load_dwordx4 v[6:9], v[14:15], off offset:16
	global_load_dwordx4 v[10:13], v[14:15], off offset:512
	s_nop 0
	global_load_dwordx4 v[14:17], v[14:15], off offset:528
	s_and_b64 vcc, exec, s[16:17]
	s_cbranch_vccz .Lg2_noxb
	s_lshl_b32 s10, s13, 19
	v_lshlrev_b32_e32 v212, 1, v208
	v_lshlrev_b32_e32 v216, 11, v190
	v_add3_u32 v212, s10, v216, v212
	global_load_dwordx4 v[242:245], v212, s[86:87]
	v_or_b32_e32 v216, 0x100, v212
	global_load_dwordx4 v[246:249], v216, s[86:87]
	v_add_u32_e32 v241, 0x8000, v212
	global_load_dwordx4 v[182:185], v241, s[86:87]
	v_add_u32_e32 v254, 0x8100, v212
	global_load_dwordx4 v[178:181], v254, s[86:87]
	v_mov_b32_e32 v221, v211
	v_add_u32_e32 v211, 0x10000, v212
	global_load_dwordx4 v[174:177], v211, s[86:87]
	v_add_u32_e32 v240, 0x10100, v212
	global_load_dwordx4 v[170:173], v240, s[86:87]
	v_add_u32_e32 v239, 0x18000, v212
	global_load_dwordx4 v[166:169], v239, s[86:87]
	v_add_u32_e32 v238, 0x18100, v212
	global_load_dwordx4 v[162:165], v238, s[86:87]
	s_waitcnt vmcnt(8)
	v_pk_mul_f32 v[200:201], v[8:9], s[46:47] op_sel_hi:[1,0]
	v_pk_mul_f32 v[204:205], v[4:5], s[46:47] op_sel_hi:[1,0]
	v_pk_mul_f32 v[206:207], v[2:3], s[46:47] op_sel_hi:[1,0]
	v_pk_mul_f32 v[202:203], v[6:7], s[46:47] op_sel_hi:[1,0]
	v_pk_mul_f32 v[196:197], v[12:13], s[46:47] op_sel_hi:[1,0]
	v_pk_mul_f32 v[198:199], v[10:11], s[46:47] op_sel_hi:[1,0]
	v_pk_mul_f32 v[192:193], v[16:17], s[46:47] op_sel_hi:[1,0]
	v_pk_mul_f32 v[194:195], v[14:15], s[46:47] op_sel_hi:[1,0]
	s_branch .Lg2_xb
.Lg2_noxb:
	s_waitcnt vmcnt(0)
	v_pk_mul_f32 v[200:201], v[8:9], s[46:47] op_sel_hi:[1,0]
	v_pk_mul_f32 v[204:205], v[4:5], s[46:47] op_sel_hi:[1,0]
	v_pk_mul_f32 v[206:207], v[2:3], s[46:47] op_sel_hi:[1,0]
	v_pk_mul_f32 v[202:203], v[6:7], s[46:47] op_sel_hi:[1,0]
	v_pk_mul_f32 v[196:197], v[12:13], s[46:47] op_sel_hi:[1,0]
	v_pk_mul_f32 v[198:199], v[10:11], s[46:47] op_sel_hi:[1,0]
	v_pk_mul_f32 v[192:193], v[16:17], s[46:47] op_sel_hi:[1,0]
	v_pk_mul_f32 v[194:195], v[14:15], s[46:47] op_sel_hi:[1,0]
	s_branch .LBB0_702
.Lg2_xb:
	v_add_u32_e32 v237, 0x40000, v212
	global_load_dwordx4 v[30:33], v237, s[86:87]
	v_add_u32_e32 v236, 0x40100, v212
	global_load_dwordx4 v[26:29], v236, s[86:87]
	v_add_u32_e32 v235, 0x48000, v212
	global_load_dwordx4 v[22:25], v235, s[86:87]
	v_add_u32_e32 v234, 0x48100, v212
	global_load_dwordx4 v[18:21], v234, s[86:87]
	v_add_u32_e32 v233, 0x50000, v212
	global_load_dwordx4 v[14:17], v233, s[86:87]
	v_add_u32_e32 v232, 0x50100, v212
	global_load_dwordx4 v[10:13], v232, s[86:87]
	v_add_u32_e32 v231, 0x58000, v212
	global_load_dwordx4 v[2:5], v231, s[86:87]
	v_add_u32_e32 v230, 0x58100, v212
	global_load_dwordx4 v[6:9], v230, s[86:87]
	s_waitcnt vmcnt(15)
	v_lshlrev_b32_e32 v250, 16, v242
	v_and_b32_e32 v251, 0xffff0000, v242
	v_lshlrev_b32_e32 v242, 16, v243
	v_and_b32_e32 v243, 0xffff0000, v243
	v_lshlrev_b32_e32 v252, 16, v244
	v_and_b32_e32 v253, 0xffff0000, v244
	v_lshlrev_b32_e32 v244, 16, v245
	v_and_b32_e32 v245, 0xffff0000, v245
	v_pk_fma_f32 v[214:215], v[160:161], v[204:205], v[242:243]
	v_pk_fma_f32 v[242:243], v[158:159], v[206:207], v[250:251]
	v_pk_fma_f32 v[250:251], v[156:157], v[200:201], v[244:245]
	v_pk_fma_f32 v[244:245], v[154:155], v[202:203], v[252:253]
	v_cvt_pk_bf16_f32 v242, v242, v243
	v_cvt_pk_bf16_f32 v243, v214, v215
	s_waitcnt vmcnt(14)
	v_lshlrev_b32_e32 v214, 16, v246
	v_cvt_pk_bf16_f32 v244, v244, v245
	v_cvt_pk_bf16_f32 v245, v250, v251
	global_store_dwordx4 v212, v[242:245], s[86:87]
	v_and_b32_e32 v215, 0xffff0000, v246
	v_lshlrev_b32_e32 v246, 16, v249
	v_lshlrev_b32_e32 v242, 16, v247
	v_and_b32_e32 v243, 0xffff0000, v247
	v_lshlrev_b32_e32 v244, 16, v248
	v_and_b32_e32 v245, 0xffff0000, v248
	v_and_b32_e32 v247, 0xffff0000, v249
	v_pk_fma_f32 v[248:249], v[152:153], v[196:197], v[242:243]
	v_pk_fma_f32 v[214:215], v[150:151], v[198:199], v[214:215]
	v_pk_fma_f32 v[244:245], v[146:147], v[194:195], v[244:245]
	v_cvt_pk_bf16_f32 v242, v214, v215
	v_cvt_pk_bf16_f32 v243, v248, v249
	v_pk_fma_f32 v[246:247], v[148:149], v[192:193], v[246:247]
	v_cvt_pk_bf16_f32 v244, v244, v245
	s_waitcnt vmcnt(14)
	v_lshlrev_b32_e32 v214, 16, v182
	v_cvt_pk_bf16_f32 v245, v246, v247
	global_store_dwordx4 v216, v[242:245], s[86:87]
	v_and_b32_e32 v215, 0xffff0000, v182
	v_lshlrev_b32_e32 v182, 16, v183
	v_and_b32_e32 v183, 0xffff0000, v183
	v_lshlrev_b32_e32 v242, 16, v184
	v_and_b32_e32 v243, 0xffff0000, v184
	v_lshlrev_b32_e32 v184, 16, v185
	v_and_b32_e32 v185, 0xffff0000, v185
	v_pk_fma_f32 v[244:245], v[144:145], v[204:205], v[182:183]
	v_pk_fma_f32 v[182:183], v[142:143], v[206:207], v[214:215]
	v_pk_fma_f32 v[214:215], v[140:141], v[200:201], v[184:185]
	v_pk_fma_f32 v[184:185], v[138:139], v[202:203], v[242:243]
	v_cvt_pk_bf16_f32 v182, v182, v183
	v_cvt_pk_bf16_f32 v183, v244, v245
	s_nop 0
	v_cvt_pk_bf16_f32 v184, v184, v185
	v_cvt_pk_bf16_f32 v185, v214, v215
	global_store_dwordx4 v241, v[182:185], s[86:87]
	s_waitcnt vmcnt(15)
	s_nop 0
	v_lshlrev_b32_e32 v182, 16, v178
	v_and_b32_e32 v183, 0xffff0000, v178
	v_lshlrev_b32_e32 v178, 16, v179
	v_and_b32_e32 v179, 0xffff0000, v179
	v_lshlrev_b32_e32 v184, 16, v180
	v_and_b32_e32 v185, 0xffff0000, v180
	v_lshlrev_b32_e32 v180, 16, v181
	v_and_b32_e32 v181, 0xffff0000, v181
	v_pk_fma_f32 v[214:215], v[136:137], v[196:197], v[178:179]
	v_pk_fma_f32 v[178:179], v[134:135], v[198:199], v[182:183]
	v_pk_fma_f32 v[182:183], v[132:133], v[192:193], v[180:181]
	v_pk_fma_f32 v[180:181], v[130:131], v[194:195], v[184:185]
	v_cvt_pk_bf16_f32 v178, v178, v179
	v_cvt_pk_bf16_f32 v179, v214, v215
	s_nop 0
	v_cvt_pk_bf16_f32 v180, v180, v181
	v_cvt_pk_bf16_f32 v181, v182, v183
	global_store_dwordx4 v254, v[178:181], s[86:87]
	s_waitcnt vmcnt(15)
	s_nop 0
	v_lshlrev_b32_e32 v178, 16, v174
	v_and_b32_e32 v179, 0xffff0000, v174
	v_lshlrev_b32_e32 v174, 16, v175
	v_and_b32_e32 v175, 0xffff0000, v175
	v_lshlrev_b32_e32 v180, 16, v176
	v_and_b32_e32 v181, 0xffff0000, v176
	v_lshlrev_b32_e32 v176, 16, v177
	v_and_b32_e32 v177, 0xffff0000, v177
	v_pk_fma_f32 v[182:183], v[128:129], v[204:205], v[174:175]
	v_pk_fma_f32 v[174:175], v[126:127], v[206:207], v[178:179]
	v_pk_fma_f32 v[178:179], v[124:125], v[200:201], v[176:177]
	v_pk_fma_f32 v[176:177], v[122:123], v[202:203], v[180:181]
	v_cvt_pk_bf16_f32 v174, v174, v175
	v_cvt_pk_bf16_f32 v175, v182, v183
	s_nop 0
	v_cvt_pk_bf16_f32 v176, v176, v177
	v_cvt_pk_bf16_f32 v177, v178, v179
	global_store_dwordx4 v211, v[174:177], s[86:87]
	v_mov_b32_e32 v211, v221
	s_waitcnt vmcnt(15)
	v_lshlrev_b32_e32 v174, 16, v170
	v_and_b32_e32 v175, 0xffff0000, v170
	v_lshlrev_b32_e32 v170, 16, v171
	v_and_b32_e32 v171, 0xffff0000, v171
	v_lshlrev_b32_e32 v176, 16, v172
	v_and_b32_e32 v177, 0xffff0000, v172
	v_lshlrev_b32_e32 v172, 16, v173
	v_and_b32_e32 v173, 0xffff0000, v173
	v_pk_fma_f32 v[178:179], v[120:121], v[196:197], v[170:171]
	v_pk_fma_f32 v[170:171], v[118:119], v[198:199], v[174:175]
	v_pk_fma_f32 v[174:175], v[116:117], v[192:193], v[172:173]
	v_pk_fma_f32 v[172:173], v[114:115], v[194:195], v[176:177]
	v_cvt_pk_bf16_f32 v170, v170, v171
	v_cvt_pk_bf16_f32 v171, v178, v179
	s_nop 0
	v_cvt_pk_bf16_f32 v172, v172, v173
	v_cvt_pk_bf16_f32 v173, v174, v175
	global_store_dwordx4 v240, v[170:173], s[86:87]
	s_waitcnt vmcnt(15)
	s_nop 0
	v_lshlrev_b32_e32 v170, 16, v166
	v_and_b32_e32 v171, 0xffff0000, v166
	v_lshlrev_b32_e32 v166, 16, v167
	v_and_b32_e32 v167, 0xffff0000, v167
	v_lshlrev_b32_e32 v172, 16, v168
	v_and_b32_e32 v173, 0xffff0000, v168
	v_lshlrev_b32_e32 v168, 16, v169
	v_and_b32_e32 v169, 0xffff0000, v169
	v_pk_fma_f32 v[174:175], v[112:113], v[204:205], v[166:167]
	v_pk_fma_f32 v[166:167], v[110:111], v[206:207], v[170:171]
	v_pk_fma_f32 v[170:171], v[108:109], v[200:201], v[168:169]
	v_pk_fma_f32 v[168:169], v[106:107], v[202:203], v[172:173]
	v_cvt_pk_bf16_f32 v166, v166, v167
	v_cvt_pk_bf16_f32 v167, v174, v175
	s_nop 0
	v_cvt_pk_bf16_f32 v168, v168, v169
	v_cvt_pk_bf16_f32 v169, v170, v171
	global_store_dwordx4 v239, v[166:169], s[86:87]
	s_waitcnt vmcnt(15)
	s_nop 0
	v_lshlrev_b32_e32 v166, 16, v162
	v_and_b32_e32 v167, 0xffff0000, v162
	v_lshlrev_b32_e32 v162, 16, v163
	v_and_b32_e32 v163, 0xffff0000, v163
	v_lshlrev_b32_e32 v168, 16, v164
	v_and_b32_e32 v169, 0xffff0000, v164
	v_lshlrev_b32_e32 v164, 16, v165
	v_and_b32_e32 v165, 0xffff0000, v165
	v_pk_fma_f32 v[170:171], v[104:105], v[196:197], v[162:163]
	v_pk_fma_f32 v[162:163], v[102:103], v[198:199], v[166:167]
	v_pk_fma_f32 v[166:167], v[100:101], v[192:193], v[164:165]
	v_pk_fma_f32 v[164:165], v[98:99], v[194:195], v[168:169]
	v_cvt_pk_bf16_f32 v162, v162, v163
	v_cvt_pk_bf16_f32 v163, v170, v171
	s_nop 0
	v_cvt_pk_bf16_f32 v164, v164, v165
	v_cvt_pk_bf16_f32 v165, v166, v167
	global_store_dwordx4 v238, v[162:165], s[86:87]
	s_waitcnt vmcnt(15)
	s_nop 0
	v_lshlrev_b32_e32 v162, 16, v30
	v_and_b32_e32 v163, 0xffff0000, v30
	v_lshlrev_b32_e32 v30, 16, v31
	v_and_b32_e32 v31, 0xffff0000, v31
	v_lshlrev_b32_e32 v164, 16, v32
	v_and_b32_e32 v165, 0xffff0000, v32
	v_lshlrev_b32_e32 v32, 16, v33
	v_and_b32_e32 v33, 0xffff0000, v33
	v_pk_fma_f32 v[166:167], v[96:97], v[204:205], v[30:31]
	v_pk_fma_f32 v[30:31], v[94:95], v[206:207], v[162:163]
	v_pk_fma_f32 v[162:163], v[92:93], v[200:201], v[32:33]
	v_pk_fma_f32 v[32:33], v[90:91], v[202:203], v[164:165]
	v_cvt_pk_bf16_f32 v30, v30, v31
	v_cvt_pk_bf16_f32 v31, v166, v167
	s_nop 0
	v_cvt_pk_bf16_f32 v32, v32, v33
	v_cvt_pk_bf16_f32 v33, v162, v163
	global_store_dwordx4 v237, v[30:33], s[86:87]
	s_waitcnt vmcnt(15)
	s_nop 0
	v_lshlrev_b32_e32 v30, 16, v26
	v_and_b32_e32 v31, 0xffff0000, v26
	v_lshlrev_b32_e32 v26, 16, v27
	v_and_b32_e32 v27, 0xffff0000, v27
	v_lshlrev_b32_e32 v32, 16, v28
	v_and_b32_e32 v33, 0xffff0000, v28
	v_lshlrev_b32_e32 v28, 16, v29
	v_and_b32_e32 v29, 0xffff0000, v29
	v_pk_fma_f32 v[162:163], v[88:89], v[196:197], v[26:27]
	v_pk_fma_f32 v[26:27], v[86:87], v[198:199], v[30:31]
	v_pk_fma_f32 v[30:31], v[84:85], v[192:193], v[28:29]
	v_pk_fma_f32 v[28:29], v[82:83], v[194:195], v[32:33]
	v_cvt_pk_bf16_f32 v26, v26, v27
	v_cvt_pk_bf16_f32 v27, v162, v163
	s_nop 0
	v_cvt_pk_bf16_f32 v28, v28, v29
	v_cvt_pk_bf16_f32 v29, v30, v31
	global_store_dwordx4 v236, v[26:29], s[86:87]
	s_waitcnt vmcnt(15)
	s_nop 0
	v_lshlrev_b32_e32 v26, 16, v22
	v_and_b32_e32 v27, 0xffff0000, v22
	v_lshlrev_b32_e32 v22, 16, v23
	v_and_b32_e32 v23, 0xffff0000, v23
	v_lshlrev_b32_e32 v28, 16, v24
	v_and_b32_e32 v29, 0xffff0000, v24
	v_lshlrev_b32_e32 v24, 16, v25
	v_and_b32_e32 v25, 0xffff0000, v25
	v_pk_fma_f32 v[30:31], v[80:81], v[204:205], v[22:23]
	v_pk_fma_f32 v[22:23], v[78:79], v[206:207], v[26:27]
	v_pk_fma_f32 v[26:27], v[76:77], v[200:201], v[24:25]
	v_pk_fma_f32 v[24:25], v[74:75], v[202:203], v[28:29]
	v_cvt_pk_bf16_f32 v22, v22, v23
	v_cvt_pk_bf16_f32 v23, v30, v31
	s_nop 0
	v_cvt_pk_bf16_f32 v24, v24, v25
	v_cvt_pk_bf16_f32 v25, v26, v27
	global_store_dwordx4 v235, v[22:25], s[86:87]
	s_waitcnt vmcnt(15)
	s_nop 0
	v_lshlrev_b32_e32 v22, 16, v18
	v_and_b32_e32 v23, 0xffff0000, v18
	v_lshlrev_b32_e32 v18, 16, v19
	v_and_b32_e32 v19, 0xffff0000, v19
	v_lshlrev_b32_e32 v24, 16, v20
	v_and_b32_e32 v25, 0xffff0000, v20
	v_lshlrev_b32_e32 v20, 16, v21
	v_and_b32_e32 v21, 0xffff0000, v21
	v_pk_fma_f32 v[26:27], v[64:65], v[196:197], v[18:19]
	v_pk_fma_f32 v[18:19], v[62:63], v[198:199], v[22:23]
	v_pk_fma_f32 v[22:23], v[52:53], v[192:193], v[20:21]
	v_pk_fma_f32 v[20:21], v[50:51], v[194:195], v[24:25]
	v_cvt_pk_bf16_f32 v18, v18, v19
	v_cvt_pk_bf16_f32 v19, v26, v27
	s_nop 0
	v_cvt_pk_bf16_f32 v20, v20, v21
	v_cvt_pk_bf16_f32 v21, v22, v23
	global_store_dwordx4 v234, v[18:21], s[86:87]
	s_waitcnt vmcnt(15)
	s_nop 0
	v_lshlrev_b32_e32 v18, 16, v14
	v_and_b32_e32 v19, 0xffff0000, v14
	v_lshlrev_b32_e32 v14, 16, v15
	v_and_b32_e32 v15, 0xffff0000, v15
	v_lshlrev_b32_e32 v20, 16, v16
	v_and_b32_e32 v21, 0xffff0000, v16
	v_lshlrev_b32_e32 v16, 16, v17
	v_and_b32_e32 v17, 0xffff0000, v17
	v_pk_fma_f32 v[22:23], v[60:61], v[204:205], v[14:15]
	v_pk_fma_f32 v[14:15], v[58:59], v[206:207], v[18:19]
	v_pk_fma_f32 v[18:19], v[44:45], v[200:201], v[16:17]
	v_pk_fma_f32 v[16:17], v[42:43], v[202:203], v[20:21]
	v_cvt_pk_bf16_f32 v14, v14, v15
	v_cvt_pk_bf16_f32 v15, v22, v23
	s_nop 0
	v_cvt_pk_bf16_f32 v16, v16, v17
	v_cvt_pk_bf16_f32 v17, v18, v19
	global_store_dwordx4 v233, v[14:17], s[86:87]
	s_waitcnt vmcnt(15)
	s_nop 0
	v_lshlrev_b32_e32 v14, 16, v10
	v_and_b32_e32 v15, 0xffff0000, v10
	v_lshlrev_b32_e32 v10, 16, v11
	v_and_b32_e32 v11, 0xffff0000, v11
	v_lshlrev_b32_e32 v16, 16, v12
	v_and_b32_e32 v17, 0xffff0000, v12
	v_lshlrev_b32_e32 v12, 16, v13
	v_and_b32_e32 v13, 0xffff0000, v13
	v_pk_fma_f32 v[18:19], v[72:73], v[196:197], v[10:11]
	v_pk_fma_f32 v[10:11], v[70:71], v[198:199], v[14:15]
	v_pk_fma_f32 v[14:15], v[68:69], v[192:193], v[12:13]
	v_pk_fma_f32 v[12:13], v[66:67], v[194:195], v[16:17]
	v_cvt_pk_bf16_f32 v10, v10, v11
	v_cvt_pk_bf16_f32 v11, v18, v19
	s_nop 0
	v_cvt_pk_bf16_f32 v12, v12, v13
	v_cvt_pk_bf16_f32 v13, v14, v15
	global_store_dwordx4 v232, v[10:13], s[86:87]
	s_waitcnt vmcnt(15)
	s_nop 0
	v_lshlrev_b32_e32 v10, 16, v2
	v_and_b32_e32 v11, 0xffff0000, v2
	v_lshlrev_b32_e32 v2, 16, v3
	v_and_b32_e32 v3, 0xffff0000, v3
	v_lshlrev_b32_e32 v12, 16, v4
	v_and_b32_e32 v13, 0xffff0000, v4
	v_lshlrev_b32_e32 v4, 16, v5
	v_and_b32_e32 v5, 0xffff0000, v5
	v_pk_fma_f32 v[14:15], v[40:41], v[204:205], v[2:3]
	v_pk_fma_f32 v[2:3], v[38:39], v[206:207], v[10:11]
	v_pk_fma_f32 v[10:11], v[36:37], v[200:201], v[4:5]
	v_pk_fma_f32 v[4:5], v[34:35], v[202:203], v[12:13]
	v_cvt_pk_bf16_f32 v2, v2, v3
	v_cvt_pk_bf16_f32 v3, v14, v15
	s_nop 0
	v_cvt_pk_bf16_f32 v4, v4, v5
	v_cvt_pk_bf16_f32 v5, v10, v11
	global_store_dwordx4 v231, v[2:5], s[86:87]
	s_waitcnt vmcnt(15)
	s_nop 0
	v_lshlrev_b32_e32 v2, 16, v6
	v_and_b32_e32 v3, 0xffff0000, v6
	v_lshlrev_b32_e32 v4, 16, v7
	v_and_b32_e32 v5, 0xffff0000, v7
	v_lshlrev_b32_e32 v6, 16, v8
	v_and_b32_e32 v7, 0xffff0000, v8
	v_lshlrev_b32_e32 v8, 16, v9
	v_and_b32_e32 v9, 0xffff0000, v9
	v_pk_fma_f32 v[4:5], v[56:57], v[196:197], v[4:5]
	v_pk_fma_f32 v[2:3], v[54:55], v[198:199], v[2:3]
	v_pk_fma_f32 v[8:9], v[48:49], v[192:193], v[8:9]
	v_pk_fma_f32 v[6:7], v[46:47], v[194:195], v[6:7]
	v_cvt_pk_bf16_f32 v2, v2, v3
	v_cvt_pk_bf16_f32 v3, v4, v5
	s_nop 0
	v_cvt_pk_bf16_f32 v4, v6, v7
	v_cvt_pk_bf16_f32 v5, v8, v9
	global_store_dwordx4 v230, v[2:5], s[86:87]
	s_cbranch_execz .LBB0_703
	s_and_b64 vcc, exec, s[4:5]
	s_mov_b64 s[4:5], -1
	s_cbranch_vccnz .LBB0_689
	s_branch .LBB0_708

.LBB0_778:
	s_sub_i32 s12, s67, s94
	s_add_i32 s12, s12, 7
	s_ashr_i32 s12, s12, 3
	s_cmp_lt_i32 s12, 1
	s_cbranch_scc1 .LBB0_805
	v_lshlrev_b32_e32 v80, 2, v110
	v_mov_b32_e32 v79, v170
	global_load_dwordx4 v[44:47], v80, s[10:11]
	global_load_dwordx4 v[64:67], v[140:141], off
	global_load_dwordx4 v[48:51], v179, s[10:11]
	global_load_dwordx4 v[68:71], v[140:141], off offset:1024
	global_load_dwordx4 v[52:55], v180, s[10:11]
	global_load_dwordx4 v[72:75], v[140:141], off offset:2048
	global_load_dwordx4 v[56:59], v181, s[10:11]
	global_load_dwordx4 v[30:33], v[140:141], off offset:3072
	global_load_dwordx4 v[2:5], v80, s[8:9]
	global_load_dwordx4 v[6:9], v179, s[8:9]
	global_load_dwordx4 v[10:13], v180, s[8:9]
	global_load_dwordx4 v[14:17], v181, s[8:9]
	s_mov_b32 s10, s17
	s_waitcnt vmcnt(10)
	v_pk_add_f32 v[46:47], v[46:47], 1.0 op_sel_hi:[1,0]
	v_pk_add_f32 v[44:45], v[44:45], 1.0 op_sel_hi:[1,0]
	v_pk_mul_f32 v[18:19], v[66:67], v[46:47]
	v_pk_mul_f32 v[20:21], v[64:65], v[44:45]
	s_waitcnt vmcnt(8)
	v_pk_add_f32 v[50:51], v[50:51], 1.0 op_sel_hi:[1,0]
	v_pk_add_f32 v[48:49], v[48:49], 1.0 op_sel_hi:[1,0]
	v_pk_mul_f32 v[22:23], v[70:71], v[50:51]
	v_pk_mul_f32 v[24:25], v[68:69], v[48:49]
	s_waitcnt vmcnt(6)
	v_pk_add_f32 v[54:55], v[54:55], 1.0 op_sel_hi:[1,0]
	v_pk_add_f32 v[52:53], v[52:53], 1.0 op_sel_hi:[1,0]
	v_pk_mul_f32 v[26:27], v[74:75], v[54:55]
	v_pk_mul_f32 v[28:29], v[72:73], v[52:53]
	s_waitcnt vmcnt(4)
	v_pk_add_f32 v[58:59], v[58:59], 1.0 op_sel_hi:[1,0]
	v_pk_add_f32 v[56:57], v[56:57], 1.0 op_sel_hi:[1,0]
	v_pk_mul_f32 v[56:57], v[30:31], v[56:57]
	v_pk_mul_f32 v[30:31], v[32:33], v[58:59]
	s_nop 0
	v_mov_b32_e32 v32, v56
	v_mov_b32_e32 v33, v57
	v_add_f32_e32 v36, 0, v40
	v_add_f32_e32 v36, v36, v41
	v_add_f32_e32 v36, v36, v42
	v_add_f32_e32 v36, v36, v43
	s_min_i32 s8, s16, s2
	v_add_f32_e32 v36, v36, v38
	s_ashr_i32 s9, s8, 31
	v_add_f32_e32 v36, v36, v39
	s_lshl_b64 s[8:9], s[8:9], 11
	v_add_f32_e32 v34, v36, v34
	s_add_u32 s8, s6, s8
	v_add_f32_e32 v78, v34, v35
	s_addc_u32 s9, s7, s9
	v_lshlrev_b32_e32 v34, 1, v110
	global_load_dwordx2 v[36:37], v34, s[8:9] offset:1536
	global_load_dwordx2 v[38:39], v34, s[8:9] offset:1024
	global_load_dwordx2 v[40:41], v34, s[8:9] offset:512
	global_load_dwordx2 v[42:43], v34, s[8:9]
	s_min_i32 s8, s97, s2
	s_ashr_i32 s9, s8, 31
	s_lshl_b64 s[8:9], s[8:9], 11
	s_add_u32 s8, s6, s8
	s_addc_u32 s9, s7, s9
	global_load_dwordx2 v[44:45], v34, s[8:9] offset:1536
	global_load_dwordx2 v[46:47], v34, s[8:9] offset:1024
	global_load_dwordx2 v[48:49], v34, s[8:9] offset:512
	global_load_dwordx2 v[50:51], v34, s[8:9]
	s_min_i32 s8, s94, s2
	s_ashr_i32 s9, s8, 31
	s_lshl_b64 s[8:9], s[8:9], 11
	s_add_u32 s8, s6, s8
	s_addc_u32 s9, s7, s9
	global_load_dwordx2 v[52:53], v34, s[8:9] offset:1536
	global_load_dwordx2 v[54:55], v34, s[8:9] offset:1024
	global_load_dwordx2 v[56:57], v34, s[8:9] offset:512
	global_load_dwordx2 v[58:59], v34, s[8:9]
	v_mov_b32_e32 v35, v0
	v_lshl_add_u64 v[34:35], s[6:7], 0, v[34:35]
	s_mov_b32 s8, 0
	s_mov_b32 s9, s18
	s_branch .LBB0_783
